# s20 + scan workgroup pairs (eh 0/1 of one batch/head/direction) placed on one XCD
# speedup vs baseline: 1.0104x; 1.0021x over previous
; #define LBAR() do { asm volatile("s_waitcnt lgkmcnt(0)" ::: "memory"); __builtin_amdgcn_s_barrier(); asm volatile("" ::: "memory"); } while (0)
; __global__ void __launch_bounds__(NTHREADS, 2) fwd(Args args) {
;     ...
;             const int bhd = bid >> 1, eh = bid & 1, b = bhd >> 3, h = (bhd >> 1) & 3, dir = bhd & 1;
;             const bf16* QEg = dir ? QEB : QEF; const bf16* KDg = dir ? KDB : KDF; const float* DECg = dir ? DECB : DECF; bf16* O = dir ? OB : OF;
;     ...
;                 const int ws = eh * 4 + wave, r = lane & 31, hh = lane >> 5;
;                 __builtin_amdgcn_s_setprio(2);
;                 typedef float f32x16 __attribute__((ext_vector_type(16)));
;                 f32x16 S[4];
; #pragma unroll
;                 for (int dt = 0; dt < 4; ++dt)
; #pragma unroll
;                     for (int i = 0; i < 16; ++i) S[dt][i] = 0.f;
;                 LBAR();
.LBB0_479:
	s_and_b64 vcc, exec, s[4:5]
	s_cbranch_vccz .LBB0_520
	s_bitcmp0_b32 s94, 0
	s_mov_b32 s2, 0
	s_cselect_b64 s[4:5], -1, 0
	s_cmpk_lt_u32 s51, 0x100
	s_mov_b64 s[6:7], -1
	s_cbranch_scc0 .LBB0_488
	s_waitcnt vmcnt(0)
	v_and_b32_e32 v2, 31, v0
	s_setprio 2
	v_readlane_b32 s3, v246, 21
	v_lshrrev_b32_e32 v3, 5, v220
	s_waitcnt lgkmcnt(0)
	s_barrier
	v_lshl_or_b32 v4, s3, 5, v2
	s_movk_i32 s3, 0x90
	v_mul_lo_u32 v98, v4, s3
	s_and_b32 s3, s51, 0xc0
	s_add_i32 s3, s3, 0
	v_lshlrev_b32_e32 v99, 4, v3
	v_lshl_add_u32 v100, v3, 3, s3
	v_or_b32_e32 v3, 32, v2
	v_mul_u32_u24_e32 v101, 0x110, v2
	v_mul_u32_u24_e32 v102, 0x108, v2
	v_mul_u32_u24_e32 v103, 0x90, v2
	v_mov_b32_e32 v2, 0
	v_mul_u32_u24_e32 v104, 0x90, v3
	s_mov_b32 s3, 0x1b000
	s_mov_b32 s8, 0
	v_mov_b32_e32 v3, v2
	v_mov_b32_e32 v4, v2
	v_mov_b32_e32 v5, v2
	v_mov_b32_e32 v6, v2
	v_mov_b32_e32 v7, v2
	v_mov_b32_e32 v8, v2
	v_mov_b32_e32 v9, v2
	v_mov_b32_e32 v10, v2
	v_mov_b32_e32 v11, v2
	v_mov_b32_e32 v12, v2
	v_mov_b32_e32 v13, v2
	v_mov_b32_e32 v14, v2
	v_mov_b32_e32 v15, v2
	v_mov_b32_e32 v16, v2
	v_mov_b32_e32 v17, v2
	v_mov_b32_e32 v18, v2
	v_mov_b32_e32 v19, v2
	v_mov_b32_e32 v20, v2
	v_mov_b32_e32 v21, v2
	v_mov_b32_e32 v22, v2
	v_mov_b32_e32 v23, v2
	v_mov_b32_e32 v24, v2
	v_mov_b32_e32 v25, v2
	v_mov_b32_e32 v26, v2
	v_mov_b32_e32 v27, v2
	v_mov_b32_e32 v28, v2
	v_mov_b32_e32 v29, v2
	v_mov_b32_e32 v30, v2
	v_mov_b32_e32 v31, v2
	v_mov_b32_e32 v32, v2
	v_mov_b32_e32 v33, v2
	v_mov_b32_e32 v34, v2
	v_mov_b32_e32 v35, v2
	v_mov_b32_e32 v36, v2
	v_mov_b32_e32 v37, v2
	v_mov_b32_e32 v38, v2
	v_mov_b32_e32 v39, v2
	v_mov_b32_e32 v40, v2
	v_mov_b32_e32 v41, v2
	v_mov_b32_e32 v42, v2
	v_mov_b32_e32 v43, v2
	v_mov_b32_e32 v44, v2
	v_mov_b32_e32 v45, v2
	v_mov_b32_e32 v46, v2
	v_mov_b32_e32 v47, v2
	v_mov_b32_e32 v48, v2
	v_mov_b32_e32 v49, v2
	v_mov_b32_e32 v50, v2
	v_mov_b32_e32 v51, v2
	v_mov_b32_e32 v52, v2
	v_mov_b32_e32 v53, v2
	v_mov_b32_e32 v54, v2
	v_mov_b32_e32 v55, v2
	v_mov_b32_e32 v56, v2
	v_mov_b32_e32 v57, v2
	v_mov_b32_e32 v58, v2
	v_mov_b32_e32 v59, v2
	v_mov_b32_e32 v60, v2
	v_mov_b32_e32 v61, v2
	v_mov_b32_e32 v62, v2
	v_mov_b32_e32 v63, v2
	v_mov_b32_e32 v64, v2
	v_mov_b32_e32 v65, v2
	s_branch .LBB0_483

; __global__ void __launch_bounds__(NTHREADS, 2) fwd(Args args) {
;     ...
;             const int bhd = bid >> 1, eh = bid & 1, b = bhd >> 3, h = (bhd >> 1) & 3, dir = bhd & 1;
;             const bf16* QEg = dir ? QEB : QEF; const bf16* KDg = dir ? KDB : KDF; const float* DECg = dir ? DECB : DECF; bf16* O = dir ? OB : OF;
;             constexpr int GBUF = 55296;
;             constexpr int OL0 = 2 * GBUF, OL1 = 139264;
;             if (wave >= 4) {
;                 const int pt = tid - 256;
;                 u32x4 R0_[13], R1_[13], R2_[13];
;     ...
;                 G2_PLOAD(R0_, 0); G2_PLOAD(R1_, 1); G2_PLOAD(R2_, 2); G2_PSTORE(R0_, 0); G2_PLOAD(R0_, 3);
.LBB0_488:
	s_and_b64 vcc, exec, s[6:7]
	s_cbranch_vccz .LBB0_520
	s_add_u32 s6, s88, 0x67000000
	s_addc_u32 s7, s89, 0
	s_add_u32 s8, s88, 0x6a600000
	s_addc_u32 s9, s89, 0
	s_add_u32 s15, s88, 0x65e00000
	s_addc_u32 s18, s89, 0
	s_add_u32 s19, s88, 0x6a700000
	s_addc_u32 s20, s89, 0
	s_bfe_u32 s22, s94, 0x10003
	s_ashr_i32 s23, s94, 4
	s_bfe_u32 s14, s94, 0x20001
	s_and_b64 s[2:3], s[4:5], exec
	s_cselect_b32 s2, s18, s7
	s_cselect_b32 s3, s15, s6
	s_cselect_b32 s9, s9, s20
	s_cselect_b32 s8, s8, s19
	s_add_u32 s24, s88, 0x68200000
	s_addc_u32 s25, s89, 0
	s_and_b64 s[6:7], s[4:5], exec
	s_cselect_b32 s6, 0, 3
	s_mul_i32 s28, s23, 0x44
	s_or_b32 s6, s6, s28
	s_ashr_i32 s7, s6, 31
	s_lshl_b64 s[18:19], s[6:7], 2
	s_or_b32 s18, s18, s14
	s_lshl_b64 s[6:7], s[18:19], 14
	s_add_u32 s6, s3, s6
	s_addc_u32 s7, s2, s7
	s_lshl_b32 s26, s22, 13
	s_lshl_b64 s[20:21], s[18:19], 15
	s_waitcnt vmcnt(0)
	v_add_u32_e32 v80, 0xffffff00, v0
	s_add_u32 s15, s24, s20
	s_addc_u32 s21, s25, s21
	s_lshl_b32 s27, s22, 14
	v_ashrrev_i32_e32 v81, 31, v80
	s_add_u32 s20, s15, s27
	v_lshlrev_b64 v[158:159], 4, v[80:81]
	s_addc_u32 s21, s21, 0
	v_lshl_add_u64 v[2:3], s[6:7], 0, v[158:159]
	v_add_u32_e32 v83, 0x100, v0
	v_or_b32_e32 v88, 0x200, v0
	global_load_dwordx4 v[76:79], v[2:3], off
	v_lshl_add_u64 v[2:3], s[20:21], 0, v[158:159]
	v_lshlrev_b32_e32 v160, 4, v0
	v_lshlrev_b32_e32 v162, 4, v83
	v_lshlrev_b32_e32 v164, 4, v88
	global_load_dwordx4 v[84:87], v[2:3], off
	global_load_dwordx4 v[92:95], v160, s[6:7]
	global_load_dwordx4 v[100:103], v160, s[20:21]
	global_load_dwordx4 v[104:107], v162, s[6:7]
	global_load_dwordx4 v[118:121], v162, s[20:21]
	global_load_dwordx4 v[122:125], v164, s[6:7]
	global_load_dwordx4 v[126:129], v164, s[20:21]
	s_and_b64 s[6:7], s[4:5], exec
	s_cselect_b32 s6, 1, 2
	s_or_b32 s6, s6, s28
	s_ashr_i32 s7, s6, 31
	s_lshl_b64 s[6:7], s[6:7], 2
	s_or_b32 s6, s6, s14
	s_lshl_b64 s[20:21], s[6:7], 14
	s_add_u32 s20, s3, s20
	s_addc_u32 s21, s2, s21
	s_lshl_b64 s[30:31], s[6:7], 15
	s_add_u32 s15, s24, s30
	s_addc_u32 s29, s25, s31
	s_add_u32 s30, s15, s27
	s_addc_u32 s31, s29, 0
	s_lshl_b64 s[6:7], s[6:7], 9
	s_add_u32 s6, s8, s6
	v_lshl_add_u64 v[2:3], s[20:21], 0, v[158:159]
	v_lshl_add_u64 v[6:7], s[30:31], 0, v[158:159]
	s_addc_u32 s7, s9, s7
	global_load_dwordx4 v[2:5], v[2:3], off
	s_nop 0
	global_load_dwordx4 v[6:9], v[6:7], off
	s_nop 0
	global_load_dwordx4 v[22:25], v160, s[20:21]
	global_load_dwordx4 v[18:21], v160, s[30:31]
	global_load_dwordx4 v[54:57], v162, s[20:21]
	global_load_dwordx4 v[46:49], v162, s[30:31]
	global_load_dwordx4 v[66:69], v164, s[20:21]
	global_load_dwordx4 v[62:65], v164, s[30:31]
	s_and_b64 s[20:21], s[4:5], exec
	s_cselect_b32 s15, 2, 1
	s_or_b32 s20, s15, s28
	s_ashr_i32 s21, s20, 31
	s_lshl_b64 s[20:21], s[20:21], 2
	s_or_b32 s20, s20, s14
	s_lshl_b64 s[30:31], s[20:21], 14
	s_add_u32 s30, s3, s30
	s_addc_u32 s31, s2, s31
	s_lshl_b64 s[34:35], s[20:21], 15
	s_add_u32 s15, s24, s34
	s_addc_u32 s29, s25, s35
	s_add_u32 s34, s15, s27
	v_and_b32_e32 v10, 0x7c, v194
	s_addc_u32 s35, s29, 0
	v_lshlrev_b32_e32 v110, 2, v10
	v_lshl_add_u64 v[10:11], s[30:31], 0, v[158:159]
	v_lshl_add_u64 v[14:15], s[34:35], 0, v[158:159]
	global_load_dwordx4 v[10:13], v[10:11], off
	s_nop 0
	global_load_dwordx4 v[14:17], v[14:15], off
	s_nop 0
	global_load_dwordx4 v[26:29], v160, s[30:31]
	global_load_dwordx4 v[30:33], v160, s[34:35]
	global_load_dwordx4 v[34:37], v162, s[30:31]
	global_load_dwordx4 v[38:41], v162, s[34:35]
	global_load_dwordx4 v[42:45], v164, s[30:31]
	global_load_dwordx4 v[50:53], v164, s[34:35]
	s_lshl_b64 s[20:21], s[20:21], 9
	s_add_u32 s20, s8, s20
	s_addc_u32 s21, s9, s21
	global_load_dwordx4 v[70:73], v110, s[6:7]
	global_load_dwordx4 v[58:61], v110, s[20:21]
	s_mov_b32 s15, 0
	v_and_b32_e32 v186, 0xf0, v160
	s_mov_b32 s38, s15
	s_mov_b32 s39, s15
	v_add_u32_e32 v177, 0, v186
	v_and_b32_e32 v184, 0x70, v160
	v_ashrrev_i32_e32 v112, 4, v80
	s_movk_i32 s6, 0x110
	s_mov_b32 s36, s15
	s_mov_b32 s37, s15
	v_mov_b64_e32 v[132:133], s[38:39]
	v_lshlrev_b64 v[74:75], 3, v[80:81]
	v_add_u32_e32 v81, 0, v184
	v_mad_i32_i24 v89, v112, s6, v177
	v_mov_b64_e32 v[130:131], s[36:37]
	v_lshrrev_b32_e32 v111, 3, v80
	s_movk_i32 s7, 0x90
	ds_write_b128 v89, v[130:133]
	v_mad_i32_i24 v89, v111, s7, v81
	v_lshrrev_b32_e32 v114, 4, v0
	s_waitcnt vmcnt(25)
	ds_write_b128 v89, v[76:79] offset:17408
	s_waitcnt vmcnt(24)
	ds_write_b128 v89, v[84:87] offset:36352
	v_mad_u32_u24 v76, v114, s6, v177
	v_lshrrev_b32_e32 v113, 3, v0
	ds_write_b128 v76, v[130:133]
	v_mad_u32_u24 v76, v113, s7, v81
	v_lshrrev_b32_e32 v115, 4, v83
	s_waitcnt vmcnt(23)
	ds_write_b128 v76, v[92:95] offset:17408
	s_waitcnt vmcnt(22)
	ds_write_b128 v76, v[100:103] offset:36352
	v_mad_u32_u24 v76, v115, s6, v177
	v_lshrrev_b32_e32 v117, 3, v83
	ds_write_b128 v76, v[130:133]
	v_mad_u32_u24 v76, v117, s7, v81
	v_lshrrev_b32_e32 v116, 4, v88
	s_waitcnt vmcnt(21)
	ds_write_b128 v76, v[104:107] offset:17408
	s_waitcnt vmcnt(20)
	ds_write_b128 v76, v[118:121] offset:36352
	v_mad_u32_u24 v76, v116, s6, v177
	v_lshrrev_b32_e32 v118, 3, v88
	s_movk_i32 s6, 0x120
	v_lshlrev_b32_e32 v190, 4, v80
	v_mov_b32_e32 v161, 0
	v_lshlrev_b32_e32 v82, 3, v0
	v_lshlrev_b32_e32 v90, 3, v83
	v_lshlrev_b32_e32 v98, 3, v88
	ds_write_b128 v76, v[130:133]
	v_mad_u32_u24 v76, v118, s7, v81
	v_cmp_gt_u32_e64 s[6:7], s6, v0
	v_add_u32_e32 v185, 0, v190
	s_waitcnt vmcnt(19)
	ds_write_b128 v76, v[122:125] offset:17408
	s_waitcnt vmcnt(18)
	ds_write_b128 v76, v[126:129] offset:36352
	s_and_saveexec_b64 s[20:21], s[6:7]
	s_cbranch_execz .LBB0_491
	s_lshl_b64 s[18:19], s[18:19], 9
	s_add_u32 s18, s8, s18
	s_addc_u32 s19, s9, s19
	global_load_dwordx4 v[76:79], v110, s[18:19]
	s_waitcnt vmcnt(0)
	ds_write_b128 v185, v[76:79] offset:35840
